# attention tile loop: all 8 K-fragment ds_reads up front, QK^T as 8 back-to-back MFMAs, next-tile ds_write staging + global loads moved behind QK^T, no negm copy
# speedup vs baseline: 1.0222x; 1.0222x over previous
; #define LAS __attribute__((address_space(3)))
; __device__ __forceinline__ int crow(int r, int hi) { return (r & 3) + 8 * (r >> 2) + 4 * hi; }
; #define AT_LOAD(j) do { _Pragma("unroll") for (int i = 0; i < 2; ++i) { const int id = tid + 512 * i, row = id >> 4, c16 = id & 15; \
;         rk[i] = *(const u32x4*)(kbase + (size_t)(64 * (j) + row) * PW + c16 * 8); rv[i] = *(const u32x4*)(vbase + (size_t)(64 * (j) + row) * PW + c16 * 8); } } while (0)
; __device__ __forceinline__ void attn_unit(const Frame& F, const bf16* __restrict__ proj, bf16* mix, const float* relb, const float* subg, int h, int qb, float lam, float one_m_li) {
;     ...
;     for (int j = 0; j < NT; ++j) {
;         const int cur = j & 1;
;         bf16x8 kf[2][2];
;         const LAS unsigned char* Kb = lds + cur * STAGE + m * 8192;
;         if (j <= cw) {
; #pragma unroll
;             for (int d0 = 0; d0 < 2; ++d0) { const int c = 2 * d0 + hi; kf[d0][0] = *(const LAS bf16x8*)(Kb + c * 1024 + ((r32 ^ c) * 16)); kf[d0][1] = *(const LAS bf16x8*)(Kb + c * 1024 + ((r32 ^ c) * 16) + 512); } }
;         __builtin_amdgcn_sched_barrier(0);
;         if (j + 1 < NT) AT_STORE(cur ^ 1);
;         if (j + 2 < NT) AT_LOAD(j + 2);
;         if (j <= cw) {
;             f32x16 p0, p1;
; #pragma unroll
;             for (int d0 = 0; d0 < 4; ++d0) { const int c = 2 * d0 + hi;
;                 const bf16x8 a0 = (d0 < 2) ? kf[d0 & 1][0] : *(const LAS bf16x8*)(Kb + c * 1024 + ((r32 ^ c) * 16));
;                 const bf16x8 a1 = (d0 < 2) ? kf[d0 & 1][1] : *(const LAS bf16x8*)(Kb + c * 1024 + ((r32 ^ c) * 16) + 512);
;                 if (d0 == 0) { p0 = __builtin_amdgcn_mfma_f32_32x32x16_bf16(a0, qr[0], negm, 0, 0, 0); p1 = __builtin_amdgcn_mfma_f32_32x32x16_bf16(a1, qr[0], negm, 0, 0, 0); }
;                 else { p0 = __builtin_amdgcn_mfma_f32_32x32x16_bf16(a0, qr[d0], p0, 0, 0, 0); p1 = __builtin_amdgcn_mfma_f32_32x32x16_bf16(a1, qr[d0], p1, 0, 0, 0); } }
;             if (j >= cw - 2) {
;                 const int base = 64 * j - qrow + 192;
; #pragma unroll
;                 for (int r = 0; r < 16; ++r) { const int kv = crow(r, hi); p0[r] += lut[base + kv]; p1[r] += lut[base + kv + 32]; }
.LBB0_581:
	s_and_b32 s88, s73, 0x8000
	s_add_i32 s79, s88, 0
	s_add_i32 s86, s13, -1
	s_add_i32 s87, s79, s40
	s_cmp_gt_u32 s86, s10
	s_cbranch_scc1 .Latt_idle
	v_add3_u32 v81, s87, v209, v210
	v_add3_u32 v80, s87, v211, v212
	v_add3_u32 v172, s87, v214, v215
	v_add3_u32 v173, s87, v216, v217
	ds_read_b128 v[144:147], v81
	ds_read_b128 v[148:151], v81 offset:512
	ds_read_b128 v[152:155], v80
	ds_read_b128 v[156:159], v80 offset:512
	ds_read_b128 v[168:171], v172
	ds_read_b128 v[176:179], v172 offset:512
	ds_read_b128 v[180:183], v173
	ds_read_b128 v[196:199], v173 offset:512
	s_waitcnt lgkmcnt(7)
	v_mfma_f32_32x32x16_bf16 v[96:111], v[144:147], v[112:115], v[64:79]
	s_waitcnt lgkmcnt(6)
	v_mfma_f32_32x32x16_bf16 v[80:95], v[148:151], v[112:115], v[64:79]
	s_waitcnt lgkmcnt(5)
	v_mfma_f32_32x32x16_bf16 v[96:111], v[152:155], v[116:119], v[96:111]
	s_waitcnt lgkmcnt(4)
	v_mfma_f32_32x32x16_bf16 v[80:95], v[156:159], v[116:119], v[80:95]
	s_waitcnt lgkmcnt(3)
	v_mfma_f32_32x32x16_bf16 v[96:111], v[168:171], v[120:123], v[96:111]
	s_waitcnt lgkmcnt(2)
	v_mfma_f32_32x32x16_bf16 v[80:95], v[176:179], v[120:123], v[80:95]
	s_waitcnt lgkmcnt(1)
	v_mfma_f32_32x32x16_bf16 v[96:111], v[180:183], v[124:127], v[96:111]
	s_waitcnt lgkmcnt(0)
	v_mfma_f32_32x32x16_bf16 v[80:95], v[196:199], v[124:127], v[80:95]
	s_cmp_ge_u32 s13, s14
	s_cbranch_scc1 .Latt_nostage
	s_xor_b32 s88, s88, 0x8000
	v_add3_u32 v146, s88, v189, v190
	v_add3_u32 v144, s88, v191, v204
	v_add_u32_e32 v147, v146, v207
	v_add_u32_e32 v146, v146, v205
	v_add_u32_e32 v145, v144, v208
	v_add_u32_e32 v144, v144, v206
	s_waitcnt vmcnt(3)
	ds_write_b128 v146, v[128:131]
	s_waitcnt vmcnt(2)
	ds_write_b128 v144, v[132:135] offset:16384
	s_waitcnt vmcnt(1)
	ds_write_b128 v147, v[136:139]
	s_waitcnt vmcnt(0)
	ds_write_b128 v145, v[140:143] offset:16384
	s_cmp_ge_u32 s86, s12
	s_cbranch_scc1 .Latt_st_done
	v_lshl_add_u64 v[144:145], v[164:165], 0, s[50:51]
	v_add_co_u32_e32 v146, vcc, 0x392b1000, v144
	s_nop 1
	v_addc_co_u32_e32 v147, vcc, 0, v145, vcc
	v_add_co_u32_e32 v144, vcc, 0x392b2000, v144
	s_nop 1
	v_addc_co_u32_e32 v145, vcc, 0, v145, vcc
	global_load_dwordx4 v[128:131], v[146:147], off offset:3072
	global_load_dwordx4 v[132:135], v[144:145], off
	v_lshl_add_u64 v[144:145], v[166:167], 0, s[50:51]
	v_add_co_u32_e32 v146, vcc, 0x392b1000, v144
	s_nop 1
	v_addc_co_u32_e32 v147, vcc, 0, v145, vcc
	v_add_co_u32_e32 v144, vcc, 0x392b2000, v144
	s_nop 1
	v_addc_co_u32_e32 v145, vcc, 0, v145, vcc
	global_load_dwordx4 v[136:139], v[146:147], off offset:3072
	global_load_dwordx4 v[140:143], v[144:145], off
.Latt_st_done:
	s_cmp_lt_i32 s86, s11
	s_cbranch_scc1 .LBB0_590
	v_add_u32_e32 v223, s60, v222
	v_add_u32_e32 v168, 0x10500, v223
	v_add_u32_e32 v170, 0x10580, v223
	ds_read2_b32 v[168:169], v168 offset1:1
	ds_read2_b32 v[170:171], v170 offset1:1
	v_add_u32_e32 v172, 0x10508, v223
	v_add_u32_e32 v174, 0x10588, v223
	v_add_u32_e32 v176, 0x10520, v223
	v_add_u32_e32 v178, 0x105a0, v223
	v_add_u32_e32 v180, 0x10528, v223
	v_add_u32_e32 v182, 0x105a8, v223
	v_add_u32_e32 v184, 0x10540, v223
	v_add_u32_e32 v196, 0x105c0, v223
	v_add_u32_e32 v198, 0x10548, v223
	v_add_u32_e32 v200, 0x105c8, v223
	v_add_u32_e32 v202, 0x10560, v223
	v_add_u32_e32 v224, 0x105e0, v223
	v_add_u32_e32 v226, 0x10568, v223
	v_add_u32_e32 v223, 0x105e8, v223
	ds_read2_b32 v[172:173], v172 offset1:1
	ds_read2_b32 v[174:175], v174 offset1:1
	ds_read2_b32 v[176:177], v176 offset1:1
	ds_read2_b32 v[178:179], v178 offset1:1
	ds_read2_b32 v[180:181], v180 offset1:1
	ds_read2_b32 v[182:183], v182 offset1:1
	ds_read2_b32 v[184:185], v184 offset1:1
	ds_read2_b32 v[196:197], v196 offset1:1
	ds_read2_b32 v[198:199], v198 offset1:1
	ds_read2_b32 v[200:201], v200 offset1:1
	ds_read2_b32 v[202:203], v202 offset1:1
	ds_read2_b32 v[224:225], v224 offset1:1
	ds_read2_b32 v[226:227], v226 offset1:1
	s_waitcnt lgkmcnt(14)
	v_pk_add_f32 v[96:97], v[96:97], v[168:169]
	ds_read2_b32 v[168:169], v223 offset1:1
	s_waitcnt lgkmcnt(3)
	v_pk_add_f32 v[108:109], v[108:109], v[202:203]
	v_pk_add_f32 v[106:107], v[106:107], v[198:199]
	s_waitcnt lgkmcnt(1)
	v_pk_add_f32 v[110:111], v[110:111], v[226:227]
	v_pk_add_f32 v[104:105], v[104:105], v[184:185]
	v_pk_add_f32 v[102:103], v[102:103], v[180:181]
	v_pk_add_f32 v[100:101], v[100:101], v[176:177]
	v_pk_add_f32 v[98:99], v[98:99], v[172:173]
	s_waitcnt lgkmcnt(0)
	v_pk_add_f32 v[94:95], v[94:95], v[168:169]
	v_pk_add_f32 v[92:93], v[92:93], v[224:225]
	v_pk_add_f32 v[90:91], v[90:91], v[200:201]
	v_pk_add_f32 v[88:89], v[88:89], v[196:197]
	v_pk_add_f32 v[86:87], v[86:87], v[182:183]
	v_pk_add_f32 v[84:85], v[84:85], v[178:179]
	v_pk_add_f32 v[82:83], v[82:83], v[174:175]
	v_pk_add_f32 v[80:81], v[80:81], v[170:171]
; __device__ __forceinline__ float swap_max(float v) { float r0, r1; swap32(v, r0, r1); return fmaxf(r0, r1); }
; #define AT_LOAD(j) do { _Pragma("unroll") for (int i = 0; i < 2; ++i) { const int id = tid + 512 * i, row = id >> 4, c16 = id & 15; \
;         rk[i] = *(const u32x4*)(kbase + (size_t)(64 * (j) + row) * PW + c16 * 8); rv[i] = *(const u32x4*)(vbase + (size_t)(64 * (j) + row) * PW + c16 * 8); } } while (0)
; #define AT_STORE(buf) do { _Pragma("unroll") for (int i = 0; i < 2; ++i) { const int id = tid + 512 * i, row = id >> 4, c16 = id & 15, mk = c16 >> 3, c = c16 & 7; \
;         *(LAS u32x4*)(lds + (buf) * STAGE + mk * 8192 + c * 1024 + ((row ^ c) * 16)) = rk[i]; \
;         *(LAS u32x4*)(lds + (buf) * STAGE + 16384 + (c16 >> 2) * 4096 + row * 64 + (c16 & 3) * 16) = rv[i]; } } while (0)
; __device__ __forceinline__ void attn_unit(const Frame& F, const bf16* __restrict__ proj, bf16* mix, const float* relb, const float* subg, int h, int qb, float lam, float one_m_li) {
;     ...
;         if (j + 1 < NT) AT_STORE(cur ^ 1);
;         if (j + 2 < NT) AT_LOAD(j + 2);
;     ...
;             float mx = fmaxf(fmaxf(p0[0], p0[1]), p1[0]), mb = fmaxf(fmaxf(p0[2], p0[3]), p1[1]); mx = fmaxf(fmaxf(mx, p1[2]), p1[3]);
; #pragma unroll
;             for (int r = 4; r < 16; r += 4) { mx = fmaxf(fmaxf(mx, p0[r]), p0[r + 1]); mb = fmaxf(fmaxf(mb, p0[r + 2]), p0[r + 3]); mx = fmaxf(fmaxf(mx, p1[r]), p1[r + 1]); mb = fmaxf(fmaxf(mb, p1[r + 2]), p1[r + 3]); }
;             mx = swap_max(fmaxf(mx, mb));
;             if (j == 0 || __any(mx > 8.0f)) {
;                 const float dl = (j == 0) ? mx : fmaxf(mx, 0.f); mrun += dl;
;                 const float alpha = __builtin_amdgcn_exp2f(-dl); lsum *= alpha;
; #pragma unroll
;                 for (int r = 0; r < 16; ++r) { p0[r] -= dl; p1[r] -= dl; negm[r] = -mrun; }
; #pragma unroll
;                 for (int eb = 0; eb < 4; ++eb)
; #pragma unroll
;                     for (int r = 0; r < 16; ++r) o[eb][r] *= alpha;
;             }
.LBB0_590:
	v_max_f32_e32 v168, v97, v97
	v_max_f32_e32 v169, v96, v96
	v_max_f32_e32 v168, v169, v168
	v_max3_f32 v169, v98, v99, v81
	v_max3_f32 v168, v168, v80, v82
	v_max3_f32 v168, v168, v83, v100
	v_max3_f32 v169, v169, v102, v103
	v_max3_f32 v168, v168, v101, v84
	v_max3_f32 v169, v169, v86, v87
	v_max3_f32 v168, v168, v85, v104
	v_max3_f32 v169, v169, v106, v107
	v_max3_f32 v168, v168, v105, v88
	v_max3_f32 v169, v169, v90, v91
	v_max3_f32 v168, v168, v89, v108
	v_max3_f32 v169, v169, v110, v111
	v_max3_f32 v168, v168, v109, v92
	v_max3_f32 v169, v169, v94, v95
	v_max3_f32 v168, v168, v93, v169
	v_mov_b32_e32 v169, v168
	s_nop 1
	v_permlane32_swap_b32 v168, v169
	s_mov_b32 s8, 0x41000000
	v_max_f32_e32 v169, v169, v169
	v_max_f32_e32 v168, v168, v168
	v_max_f32_e32 v168, v168, v169
	v_cmp_lt_f32_e32 vcc, s8, v168
	s_cbranch_vccz .LBB0_579
	v_max_f32_e32 v64, v168, v168
	v_max_f32_e32 v66, 0, v64
	v_exp_f32_e64 v68, -v66
	v_add_f32_e32 v162, v162, v66
	v_xor_b32_e32 v64, 0x80000000, v162
	v_pk_add_f32 v[96:97], v[96:97], v[66:67] op_sel_hi:[1,0] neg_lo:[0,1] neg_hi:[0,1]
	v_pk_add_f32 v[80:81], v[80:81], v[66:67] op_sel_hi:[1,0] neg_lo:[0,1] neg_hi:[0,1]
	v_pk_add_f32 v[98:99], v[98:99], v[66:67] op_sel_hi:[1,0] neg_lo:[0,1] neg_hi:[0,1]
	v_pk_add_f32 v[82:83], v[82:83], v[66:67] op_sel_hi:[1,0] neg_lo:[0,1] neg_hi:[0,1]
	v_pk_add_f32 v[100:101], v[100:101], v[66:67] op_sel_hi:[1,0] neg_lo:[0,1] neg_hi:[0,1]
	v_pk_add_f32 v[84:85], v[84:85], v[66:67] op_sel_hi:[1,0] neg_lo:[0,1] neg_hi:[0,1]
	v_pk_add_f32 v[102:103], v[102:103], v[66:67] op_sel_hi:[1,0] neg_lo:[0,1] neg_hi:[0,1]
	v_pk_add_f32 v[86:87], v[86:87], v[66:67] op_sel_hi:[1,0] neg_lo:[0,1] neg_hi:[0,1]
	v_pk_add_f32 v[104:105], v[104:105], v[66:67] op_sel_hi:[1,0] neg_lo:[0,1] neg_hi:[0,1]
	v_pk_add_f32 v[88:89], v[88:89], v[66:67] op_sel_hi:[1,0] neg_lo:[0,1] neg_hi:[0,1]
	v_pk_add_f32 v[106:107], v[106:107], v[66:67] op_sel_hi:[1,0] neg_lo:[0,1] neg_hi:[0,1]
	v_pk_add_f32 v[90:91], v[90:91], v[66:67] op_sel_hi:[1,0] neg_lo:[0,1] neg_hi:[0,1]
	v_pk_add_f32 v[108:109], v[108:109], v[66:67] op_sel_hi:[1,0] neg_lo:[0,1] neg_hi:[0,1]
	v_pk_add_f32 v[92:93], v[92:93], v[66:67] op_sel_hi:[1,0] neg_lo:[0,1] neg_hi:[0,1]
	v_pk_add_f32 v[110:111], v[110:111], v[66:67] op_sel_hi:[1,0] neg_lo:[0,1] neg_hi:[0,1]
	v_pk_add_f32 v[94:95], v[94:95], v[66:67] op_sel_hi:[1,0] neg_lo:[0,1] neg_hi:[0,1]
	v_pk_mul_f32 v[62:63], v[62:63], v[68:69] op_sel_hi:[1,0]
	v_pk_mul_f32 v[60:61], v[60:61], v[68:69] op_sel_hi:[1,0]
	v_pk_mul_f32 v[58:59], v[58:59], v[68:69] op_sel_hi:[1,0]
	v_pk_mul_f32 v[56:57], v[56:57], v[68:69] op_sel_hi:[1,0]
	v_pk_mul_f32 v[54:55], v[54:55], v[68:69] op_sel_hi:[1,0]
	v_pk_mul_f32 v[52:53], v[52:53], v[68:69] op_sel_hi:[1,0]
	v_pk_mul_f32 v[50:51], v[50:51], v[68:69] op_sel_hi:[1,0]
	v_pk_mul_f32 v[48:49], v[48:49], v[68:69] op_sel_hi:[1,0]
	v_pk_mul_f32 v[46:47], v[46:47], v[68:69] op_sel_hi:[1,0]
	v_pk_mul_f32 v[44:45], v[44:45], v[68:69] op_sel_hi:[1,0]
	v_pk_mul_f32 v[42:43], v[42:43], v[68:69] op_sel_hi:[1,0]
	v_pk_mul_f32 v[40:41], v[40:41], v[68:69] op_sel_hi:[1,0]
	v_pk_mul_f32 v[38:39], v[38:39], v[68:69] op_sel_hi:[1,0]
	v_pk_mul_f32 v[36:37], v[36:37], v[68:69] op_sel_hi:[1,0]
	v_pk_mul_f32 v[34:35], v[34:35], v[68:69] op_sel_hi:[1,0]
	v_pk_mul_f32 v[32:33], v[32:33], v[68:69] op_sel_hi:[1,0]
	v_pk_mul_f32 v[30:31], v[30:31], v[68:69] op_sel_hi:[1,0]
	v_pk_mul_f32 v[28:29], v[28:29], v[68:69] op_sel_hi:[1,0]
	v_pk_mul_f32 v[26:27], v[26:27], v[68:69] op_sel_hi:[1,0]
	v_pk_mul_f32 v[24:25], v[24:25], v[68:69] op_sel_hi:[1,0]
	v_pk_mul_f32 v[22:23], v[22:23], v[68:69] op_sel_hi:[1,0]
	v_pk_mul_f32 v[20:21], v[20:21], v[68:69] op_sel_hi:[1,0]
	v_pk_mul_f32 v[18:19], v[18:19], v[68:69] op_sel_hi:[1,0]
	v_pk_mul_f32 v[16:17], v[16:17], v[68:69] op_sel_hi:[1,0]
	v_pk_mul_f32 v[14:15], v[14:15], v[68:69] op_sel_hi:[1,0]
	v_pk_mul_f32 v[12:13], v[12:13], v[68:69] op_sel_hi:[1,0]
	v_pk_mul_f32 v[10:11], v[10:11], v[68:69] op_sel_hi:[1,0]
	v_pk_mul_f32 v[8:9], v[8:9], v[68:69] op_sel_hi:[1,0]
	v_pk_mul_f32 v[6:7], v[6:7], v[68:69] op_sel_hi:[1,0]
	v_pk_mul_f32 v[4:5], v[4:5], v[68:69] op_sel_hi:[1,0]
	v_pk_mul_f32 v[2:3], v[2:3], v[68:69] op_sel_hi:[1,0]
	v_pk_mul_f32 v[0:1], v[0:1], v[68:69] op_sel_hi:[1,0]
	v_mul_f32_e32 v163, v163, v68
	v_mov_b32_e32 v65, v64
	v_mov_b32_e32 v66, v64
	v_mov_b32_e32 v67, v64
	v_mov_b32_e32 v68, v64
	v_mov_b32_e32 v69, v64
	v_mov_b32_e32 v70, v64
	v_mov_b32_e32 v71, v64
	v_mov_b32_e32 v72, v64
	v_mov_b32_e32 v73, v64
	v_mov_b32_e32 v74, v64
	v_mov_b32_e32 v75, v64
	v_mov_b32_e32 v76, v64
	v_mov_b32_e32 v77, v64
	v_mov_b32_e32 v78, v64
	v_mov_b32_e32 v79, v64
	s_branch .LBB0_579
.Latt_nostage:
	s_nop 7
	s_branch .Latt_st_done
.Latt_idle:
	s_cmp_ge_u32 s13, s14
	s_cbranch_scc1 .LBB0_580
	s_xor_b32 s88, s88, 0x8000
	v_add3_u32 v82, s88, v189, v190
	v_add3_u32 v80, s88, v191, v204
	v_add_u32_e32 v83, v82, v207
	v_add_u32_e32 v82, v82, v205
	v_add_u32_e32 v81, v80, v208
	v_add_u32_e32 v80, v80, v206
	s_waitcnt vmcnt(3)
	ds_write_b128 v82, v[128:131]
	s_waitcnt vmcnt(2)
	ds_write_b128 v80, v[132:135] offset:16384
	s_waitcnt vmcnt(1)
	ds_write_b128 v83, v[136:139]
	s_waitcnt vmcnt(0)
	ds_write_b128 v81, v[140:143] offset:16384
	s_cmp_ge_u32 s86, s12
	s_cbranch_scc1 .LBB0_580
	v_lshl_add_u64 v[80:81], v[164:165], 0, s[50:51]
	v_add_co_u32_e32 v82, vcc, 0x392b1000, v80
	s_nop 1
	v_addc_co_u32_e32 v83, vcc, 0, v81, vcc
	v_add_co_u32_e32 v80, vcc, 0x392b2000, v80
	s_nop 1
	v_addc_co_u32_e32 v81, vcc, 0, v81, vcc
	global_load_dwordx4 v[128:131], v[82:83], off offset:3072
	global_load_dwordx4 v[132:135], v[80:81], off
	v_lshl_add_u64 v[80:81], v[166:167], 0, s[50:51]
	v_add_co_u32_e32 v82, vcc, 0x392b1000, v80
	s_nop 1
	v_addc_co_u32_e32 v83, vcc, 0, v81, vcc
	v_add_co_u32_e32 v80, vcc, 0x392b2000, v80
	s_nop 1
	v_addc_co_u32_e32 v81, vcc, 0, v81, vcc
	global_load_dwordx4 v[136:139], v[82:83], off offset:3072
	global_load_dwordx4 v[140:143], v[80:81], off
	s_branch .LBB0_580
